# in-proj K-loop load phases: SGPR-base LDS-DMA addressing and a pre-biased LDS address register (no VALU address adds)
# speedup vs baseline: 1.0030x; 1.0030x over previous
; #define PG8_STAGE(bufoff, gbase, voff) do { _Pragma("unroll") for (int _i = 0; _i < 2; ++_i) \
;         __builtin_amdgcn_global_load_lds((const unsigned*)((const char*)(gbase) + (voff)[_i]), (LAS unsigned*)(lds + (bufoff) + ldsw + _i * 8192), 16, 0, 0); } while (0)
; #define PG8_LDA(dst, b, h) do { _Pragma("unroll") for (int m = 0; m < 4; ++m) _Pragma("unroll") for (int k = 0; k < 2; ++k) dst[m][k] = *(const LAS bf16x8*)(lds + PG8_SA(b, h) + aoff + m * 2048 + k * 1024); } while (0)
; #define PG8_LDB(dst, b, h) do { _Pragma("unroll") for (int n = 0; n < 2; ++n) _Pragma("unroll") for (int k = 0; k < 2; ++k) dst[n][k] = *(const LAS bf16x8*)(lds + PG8_SB(b, h) + boff + n * 2048 + k * 1024); } while (0)
; #define PG8_MMA(ai, bj, At, Bt) do { __builtin_amdgcn_s_setprio(1); _Pragma("unroll") for (int m = 0; m < 4; ++m) _Pragma("unroll") for (int n = 0; n < 2; ++n) _Pragma("unroll") for (int k = 0; k < 2; ++k) \
;         acc[ai][bj][m][n] = __builtin_amdgcn_mfma_f32_16x16x32_bf16(Bt[n][k], At[m][k], acc[ai][bj][m][n], 0, 0, 0); __builtin_amdgcn_s_setprio(0); } while (0)
; #define PG8_WAIT_V(n) asm volatile("s_waitcnt vmcnt(" #n ")" ::: "memory")
; #define PG8_WAIT_L(n) asm volatile("s_waitcnt lgkmcnt(" #n ")" ::: "memory")
; #define PG8_BAR __builtin_amdgcn_s_barrier()
; #define PG8_SCHED __builtin_amdgcn_sched_barrier(0)
; template <class Epi, class Sched>
; __device__ __forceinline__ void gemm_phase(LAS unsigned char* lds, const int tid, const char* Abase, const int K, const Sched& S, const Epi& E) {
;     ...
;             PG8_LDB(B0, 0, 0); PG8_LDB(B1, 0, 1); PG8_SCHED; PG8_LDA(At, 0, 0); PG8_STAGE(PG8_SA(1, 1), a1, vc[1]);
;             PG8_WAIT_V(8); PG8_WAIT_L(0); PG8_BAR; PG8_MMA(0, 0, At, B0); PG8_MMA(0, 1, At, B1); PG8_BAR; PG8_SCHED;
;     ...
; #pragma unroll
;         for (int a = 0; a < 2; ++a)
; #pragma unroll
;             for (int b = 0; b < 2; ++b)
; #pragma unroll
;                 for (int m = 0; m < 4; ++m)
; #pragma unroll
;                     for (int n = 0; n < 2; ++n) acc[a][b][m][n] = (f32x4){0.f, 0.f, 0.f, 0.f};
.LBB0_346:
	v_add_u32_e32 v241, 0x10000, v147
	s_add_u32 s7, s14, 0x100
	v_mov_b32_e32 v34, 0
	ds_write_b128 v146, v[2:5]
	v_mov_b32_e32 v117, v1
	v_mov_b32_e32 v139, v1
	s_addc_u32 s18, s15, 0
	s_mov_b32 s19, -2
	s_mov_b64 s[12:13], s[52:53]
	v_mov_b32_e32 v35, v34
	v_mov_b32_e32 v36, v34
	v_mov_b32_e32 v37, v34
	v_mov_b32_e32 v38, v34
	v_mov_b32_e32 v39, v34
	v_mov_b32_e32 v40, v34
	v_mov_b32_e32 v41, v34
	v_mov_b32_e32 v50, v34
	v_mov_b32_e32 v51, v34
	v_mov_b32_e32 v52, v34
	v_mov_b32_e32 v53, v34
	v_mov_b32_e32 v54, v34
	v_mov_b32_e32 v55, v34
	v_mov_b32_e32 v56, v34
	v_mov_b32_e32 v57, v34
	v_mov_b32_e32 v10, v34
	v_mov_b32_e32 v11, v34
	v_mov_b32_e32 v12, v34
	v_mov_b32_e32 v13, v34
	v_mov_b32_e32 v14, v34
	v_mov_b32_e32 v15, v34
	v_mov_b32_e32 v16, v34
	v_mov_b32_e32 v17, v34
	v_mov_b32_e32 v26, v34
	v_mov_b32_e32 v27, v34
	v_mov_b32_e32 v28, v34
	v_mov_b32_e32 v29, v34
	v_mov_b32_e32 v30, v34
	v_mov_b32_e32 v31, v34
	v_mov_b32_e32 v32, v34
	v_mov_b32_e32 v33, v34
	v_mov_b32_e32 v42, v34
	v_mov_b32_e32 v43, v34
	v_mov_b32_e32 v44, v34
	v_mov_b32_e32 v45, v34
	v_mov_b32_e32 v46, v34
	v_mov_b32_e32 v47, v34
	v_mov_b32_e32 v48, v34
	v_mov_b32_e32 v49, v34
	v_mov_b32_e32 v58, v34
	v_mov_b32_e32 v59, v34
	v_mov_b32_e32 v60, v34
	v_mov_b32_e32 v61, v34
	v_mov_b32_e32 v62, v34
	v_mov_b32_e32 v63, v34
	v_mov_b32_e32 v64, v34
	v_mov_b32_e32 v65, v34
	v_mov_b32_e32 v66, v34
	v_mov_b32_e32 v67, v34
	v_mov_b32_e32 v68, v34
	v_mov_b32_e32 v69, v34
	v_mov_b32_e32 v70, v34
	v_mov_b32_e32 v71, v34
	v_mov_b32_e32 v72, v34
	v_mov_b32_e32 v73, v34
	v_mov_b32_e32 v82, v34
	v_mov_b32_e32 v83, v34
	v_mov_b32_e32 v84, v34
	v_mov_b32_e32 v85, v34
	v_mov_b32_e32 v86, v34
	v_mov_b32_e32 v87, v34
	v_mov_b32_e32 v88, v34
	v_mov_b32_e32 v89, v34
	v_mov_b32_e32 v98, v34
	v_mov_b32_e32 v99, v34
	v_mov_b32_e32 v100, v34
	v_mov_b32_e32 v101, v34
	v_mov_b32_e32 v102, v34
	v_mov_b32_e32 v103, v34
	v_mov_b32_e32 v104, v34
	v_mov_b32_e32 v105, v34
	v_mov_b32_e32 v118, v34
	v_mov_b32_e32 v119, v34
	v_mov_b32_e32 v120, v34
	v_mov_b32_e32 v121, v34
	v_mov_b32_e32 v122, v34
	v_mov_b32_e32 v123, v34
	v_mov_b32_e32 v124, v34
	v_mov_b32_e32 v125, v34
	v_mov_b32_e32 v74, v34
	v_mov_b32_e32 v75, v34
	v_mov_b32_e32 v76, v34
	v_mov_b32_e32 v77, v34
	v_mov_b32_e32 v78, v34
	v_mov_b32_e32 v79, v34
	v_mov_b32_e32 v80, v34
	v_mov_b32_e32 v81, v34
	v_mov_b32_e32 v90, v34
	v_mov_b32_e32 v91, v34
	v_mov_b32_e32 v92, v34
	v_mov_b32_e32 v93, v34
	v_mov_b32_e32 v94, v34
	v_mov_b32_e32 v95, v34
	v_mov_b32_e32 v96, v34
	v_mov_b32_e32 v97, v34
	v_mov_b32_e32 v106, v34
	v_mov_b32_e32 v107, v34
	v_mov_b32_e32 v108, v34
	v_mov_b32_e32 v109, v34
	v_mov_b32_e32 v110, v34
	v_mov_b32_e32 v111, v34
	v_mov_b32_e32 v112, v34
	v_mov_b32_e32 v113, v34
	v_mov_b32_e32 v126, v34
	v_mov_b32_e32 v127, v34
	v_mov_b32_e32 v128, v34
	v_mov_b32_e32 v129, v34
	v_mov_b32_e32 v130, v34
	v_mov_b32_e32 v131, v34
	v_mov_b32_e32 v132, v34
	v_mov_b32_e32 v133, v34
	v_mov_b32_e32 v22, v34
	v_mov_b32_e32 v23, v34
	v_mov_b32_e32 v24, v34
	v_mov_b32_e32 v25, v34
	v_mov_b32_e32 v18, v34
	v_mov_b32_e32 v19, v34
	v_mov_b32_e32 v20, v34
	v_mov_b32_e32 v21, v34
	v_mov_b32_e32 v6, v34
	v_mov_b32_e32 v7, v34
	v_mov_b32_e32 v8, v34
	v_mov_b32_e32 v9, v34
	v_mov_b32_e32 v2, v34
	v_mov_b32_e32 v3, v34
	v_mov_b32_e32 v4, v34
	v_mov_b32_e32 v5, v34
	s_branch .LBB0_348
.LBB0_347:
	s_add_u32 s16, s12, 0x80
	s_addc_u32 s17, s13, 0
	s_and_b64 s[14:15], s[14:15], exec
	s_cselect_b32 s17, s31, s17
	s_cselect_b32 s16, s30, s16
	s_cselect_b32 s15, s61, s18
	s_cselect_b32 s14, s60, s7
	s_add_i32 s20, 0, 0x10000
	s_add_i32 s27, 0, 0x14000
	ds_read_b128 v[150:153], v241
	ds_read_b128 v[154:157], v241 offset:1024
	ds_read_b128 v[158:161], v241 offset:2048
	ds_read_b128 v[162:165], v241 offset:3072
	ds_read_b128 v[166:169], v241 offset:16384
	ds_read_b128 v[170:173], v241 offset:17408
	ds_read_b128 v[174:177], v241 offset:18432
	ds_read_b128 v[178:181], v241 offset:19456
	s_add_i32 m0, s71, 0xc000
	ds_read_b128 v[182:185], v148
	ds_read_b128 v[202:205], v148 offset:1024
	ds_read_b128 v[206:209], v148 offset:2048
	ds_read_b128 v[214:217], v148 offset:3072
	ds_read_b128 v[218:221], v148 offset:4096
	ds_read_b128 v[222:225], v148 offset:5120
	ds_read_b128 v[226:229], v148 offset:6144
	ds_read_b128 v[230:233], v148 offset:7168
	global_load_lds_dwordx4 v116, s[12:13]
	s_add_i32 m0, s71, 0xe000
	s_nop 0
	global_load_lds_dwordx4 v138, s[12:13]
	s_waitcnt vmcnt(8)
	s_waitcnt lgkmcnt(0)
	s_barrier
	s_setprio 1
	s_waitcnt lgkmcnt(0)
	v_mfma_f32_16x16x32_bf16 v[130:133], v[150:153], v[182:185], v[130:133]
	v_mfma_f32_16x16x32_bf16 v[126:129], v[158:161], v[182:185], v[126:129]
	v_mfma_f32_16x16x32_bf16 v[110:113], v[150:153], v[206:209], v[110:113]
	v_mfma_f32_16x16x32_bf16 v[106:109], v[158:161], v[206:209], v[106:109]
	v_mfma_f32_16x16x32_bf16 v[94:97], v[150:153], v[218:221], v[94:97]
	v_mfma_f32_16x16x32_bf16 v[90:93], v[158:161], v[218:221], v[90:93]
	v_mfma_f32_16x16x32_bf16 v[78:81], v[150:153], v[226:229], v[78:81]
	v_mfma_f32_16x16x32_bf16 v[74:77], v[158:161], v[226:229], v[74:77]
	v_mfma_f32_16x16x32_bf16 v[130:133], v[154:157], v[202:205], v[130:133]
	v_mfma_f32_16x16x32_bf16 v[126:129], v[162:165], v[202:205], v[126:129]
	v_mfma_f32_16x16x32_bf16 v[110:113], v[154:157], v[214:217], v[110:113]
	v_mfma_f32_16x16x32_bf16 v[106:109], v[162:165], v[214:217], v[106:109]
	v_mfma_f32_16x16x32_bf16 v[94:97], v[154:157], v[222:225], v[94:97]
	v_mfma_f32_16x16x32_bf16 v[90:93], v[162:165], v[222:225], v[90:93]
	v_mfma_f32_16x16x32_bf16 v[78:81], v[154:157], v[230:233], v[78:81]
	v_mfma_f32_16x16x32_bf16 v[74:77], v[162:165], v[230:233], v[74:77]
	s_setprio 0
	s_setprio 1
	v_mfma_f32_16x16x32_bf16 v[122:125], v[166:169], v[182:185], v[122:125]
	v_mfma_f32_16x16x32_bf16 v[118:121], v[174:177], v[182:185], v[118:121]
	v_mfma_f32_16x16x32_bf16 v[102:105], v[166:169], v[206:209], v[102:105]
	v_mfma_f32_16x16x32_bf16 v[98:101], v[174:177], v[206:209], v[98:101]
	v_mfma_f32_16x16x32_bf16 v[86:89], v[166:169], v[218:221], v[86:89]
	v_mfma_f32_16x16x32_bf16 v[82:85], v[174:177], v[218:221], v[82:85]
	v_mfma_f32_16x16x32_bf16 v[70:73], v[166:169], v[226:229], v[70:73]
	v_mfma_f32_16x16x32_bf16 v[66:69], v[174:177], v[226:229], v[66:69]
	v_mfma_f32_16x16x32_bf16 v[122:125], v[170:173], v[202:205], v[122:125]
	v_mfma_f32_16x16x32_bf16 v[118:121], v[178:181], v[202:205], v[118:121]
	v_mfma_f32_16x16x32_bf16 v[102:105], v[170:173], v[214:217], v[102:105]
	v_mfma_f32_16x16x32_bf16 v[98:101], v[178:181], v[214:217], v[98:101]
	v_mfma_f32_16x16x32_bf16 v[86:89], v[170:173], v[222:225], v[86:89]
	v_mfma_f32_16x16x32_bf16 v[82:85], v[178:181], v[222:225], v[82:85]
	v_mfma_f32_16x16x32_bf16 v[70:73], v[170:173], v[230:233], v[70:73]
	v_mfma_f32_16x16x32_bf16 v[66:69], v[178:181], v[230:233], v[66:69]
	s_setprio 0
	s_barrier
; #define PG8_STAGE(bufoff, gbase, voff) do { _Pragma("unroll") for (int _i = 0; _i < 2; ++_i) \
;         __builtin_amdgcn_global_load_lds((const unsigned*)((const char*)(gbase) + (voff)[_i]), (LAS unsigned*)(lds + (bufoff) + ldsw + _i * 8192), 16, 0, 0); } while (0)
; #define PG8_LDA(dst, b, h) do { _Pragma("unroll") for (int m = 0; m < 4; ++m) _Pragma("unroll") for (int k = 0; k < 2; ++k) dst[m][k] = *(const LAS bf16x8*)(lds + PG8_SA(b, h) + aoff + m * 2048 + k * 1024); } while (0)
; #define PG8_LDB(dst, b, h) do { _Pragma("unroll") for (int n = 0; n < 2; ++n) _Pragma("unroll") for (int k = 0; k < 2; ++k) dst[n][k] = *(const LAS bf16x8*)(lds + PG8_SB(b, h) + boff + n * 2048 + k * 1024); } while (0)
; #define PG8_MMA(ai, bj, At, Bt) do { __builtin_amdgcn_s_setprio(1); _Pragma("unroll") for (int m = 0; m < 4; ++m) _Pragma("unroll") for (int n = 0; n < 2; ++n) _Pragma("unroll") for (int k = 0; k < 2; ++k) \
;         acc[ai][bj][m][n] = __builtin_amdgcn_mfma_f32_16x16x32_bf16(Bt[n][k], At[m][k], acc[ai][bj][m][n], 0, 0, 0); __builtin_amdgcn_s_setprio(0); } while (0)
; #define PG8_WAIT_V(n) asm volatile("s_waitcnt vmcnt(" #n ")" ::: "memory")
; #define PG8_WAIT_L(n) asm volatile("s_waitcnt lgkmcnt(" #n ")" ::: "memory")
; #define PG8_BAR __builtin_amdgcn_s_barrier()
; #define PG8_SCHED __builtin_amdgcn_sched_barrier(0)
; template <class Epi, class Sched>
; __device__ __forceinline__ void gemm_phase(LAS unsigned char* lds, const int tid, const char* Abase, const int K, const Sched& S, const Epi& E) {
;     ...
;             PG8_LDA(At, 0, 1); PG8_STAGE(PG8_SB(0, 0), b2, voffB); PG8_STAGE(PG8_SB(0, 1), b2 + hstep, voffB); PG8_STAGE(PG8_SA(0, 0), a2, w2[0]);
;             PG8_WAIT_V(8); PG8_WAIT_L(0); PG8_BAR; PG8_MMA(1, 0, At, B0); PG8_MMA(1, 1, At, B1); PG8_BAR; PG8_SCHED;
;             PG8_LDB(B0, 1, 0); PG8_LDB(B1, 1, 1); PG8_SCHED; PG8_LDA(At, 1, 0); PG8_STAGE(PG8_SA(0, 1), a2, w2[1]);
;             PG8_WAIT_V(8); PG8_WAIT_L(0); PG8_BAR; PG8_MMA(0, 0, At, B0); PG8_MMA(0, 1, At, B1); PG8_BAR; PG8_SCHED;
	s_add_i32 s20, s20, s70
	s_mov_b32 m0, s20
	ds_read_b128 v[182:185], v148 offset:16384
	ds_read_b128 v[202:205], v148 offset:17408
	ds_read_b128 v[206:209], v148 offset:18432
	ds_read_b128 v[214:217], v148 offset:19456
	ds_read_b128 v[218:221], v148 offset:20480
	ds_read_b128 v[222:225], v148 offset:21504
	ds_read_b128 v[226:229], v148 offset:22528
	ds_read_b128 v[230:233], v148 offset:23552
	global_load_lds_dwordx4 v134, s[14:15]
	s_add_i32 m0, s20, 0x2000
	s_add_u32 s20, s14, 0x40000
	s_addc_u32 s21, s15, 0
	s_add_i32 s27, s27, s70
	global_load_lds_dwordx4 v136, s[14:15]
	s_mov_b32 m0, s27
	s_nop 0
	global_load_lds_dwordx4 v134, s[20:21]
	s_add_i32 m0, s27, 0x2000
	s_nop 0
	global_load_lds_dwordx4 v136, s[20:21]
	s_mov_b32 m0, s71
	s_nop 0
	global_load_lds_dwordx4 v0, s[16:17]
	s_mov_b32 m0, s72
	s_nop 0
	global_load_lds_dwordx4 v144, s[16:17]
	s_waitcnt vmcnt(8)
	s_waitcnt lgkmcnt(0)
	s_barrier
	s_setprio 1
	s_waitcnt lgkmcnt(0)
	v_mfma_f32_16x16x32_bf16 v[62:65], v[150:153], v[182:185], v[62:65]
	v_mfma_f32_16x16x32_bf16 v[58:61], v[158:161], v[182:185], v[58:61]
	v_mfma_f32_16x16x32_bf16 v[46:49], v[150:153], v[206:209], v[46:49]
	v_mfma_f32_16x16x32_bf16 v[42:45], v[158:161], v[206:209], v[42:45]
	v_mfma_f32_16x16x32_bf16 v[30:33], v[150:153], v[218:221], v[30:33]
	v_mfma_f32_16x16x32_bf16 v[26:29], v[158:161], v[218:221], v[26:29]
	v_mfma_f32_16x16x32_bf16 v[14:17], v[150:153], v[226:229], v[14:17]
	v_mfma_f32_16x16x32_bf16 v[10:13], v[158:161], v[226:229], v[10:13]
	v_mfma_f32_16x16x32_bf16 v[62:65], v[154:157], v[202:205], v[62:65]
	v_mfma_f32_16x16x32_bf16 v[58:61], v[162:165], v[202:205], v[58:61]
	v_mfma_f32_16x16x32_bf16 v[46:49], v[154:157], v[214:217], v[46:49]
	v_mfma_f32_16x16x32_bf16 v[42:45], v[162:165], v[214:217], v[42:45]
	v_mfma_f32_16x16x32_bf16 v[30:33], v[154:157], v[222:225], v[30:33]
	v_mfma_f32_16x16x32_bf16 v[26:29], v[162:165], v[222:225], v[26:29]
	v_mfma_f32_16x16x32_bf16 v[14:17], v[154:157], v[230:233], v[14:17]
	v_mfma_f32_16x16x32_bf16 v[10:13], v[162:165], v[230:233], v[10:13]
	s_setprio 0
	s_setprio 1
	v_mfma_f32_16x16x32_bf16 v[54:57], v[166:169], v[182:185], v[54:57]
	v_mfma_f32_16x16x32_bf16 v[50:53], v[174:177], v[182:185], v[50:53]
	v_mfma_f32_16x16x32_bf16 v[38:41], v[166:169], v[206:209], v[38:41]
	v_mfma_f32_16x16x32_bf16 v[34:37], v[174:177], v[206:209], v[34:37]
	v_mfma_f32_16x16x32_bf16 v[22:25], v[166:169], v[218:221], v[22:25]
	v_mfma_f32_16x16x32_bf16 v[18:21], v[174:177], v[218:221], v[18:21]
	v_mfma_f32_16x16x32_bf16 v[6:9], v[166:169], v[226:229], v[6:9]
	v_mfma_f32_16x16x32_bf16 v[2:5], v[174:177], v[226:229], v[2:5]
	v_mfma_f32_16x16x32_bf16 v[54:57], v[170:173], v[202:205], v[54:57]
	v_mfma_f32_16x16x32_bf16 v[50:53], v[178:181], v[202:205], v[50:53]
	v_mfma_f32_16x16x32_bf16 v[38:41], v[170:173], v[214:217], v[38:41]
	v_mfma_f32_16x16x32_bf16 v[34:37], v[178:181], v[214:217], v[34:37]
	v_mfma_f32_16x16x32_bf16 v[22:25], v[170:173], v[222:225], v[22:25]
	v_mfma_f32_16x16x32_bf16 v[18:21], v[178:181], v[222:225], v[18:21]
	v_mfma_f32_16x16x32_bf16 v[6:9], v[170:173], v[230:233], v[6:9]
	v_mfma_f32_16x16x32_bf16 v[2:5], v[178:181], v[230:233], v[2:5]
	s_setprio 0
	s_barrier
	s_add_i32 s20, 0, 0x18000
	s_add_i32 s21, 0, 0x1c000
	ds_read_b128 v[150:153], v241 offset:32768
	ds_read_b128 v[154:157], v241 offset:33792
	ds_read_b128 v[158:161], v241 offset:34816
	ds_read_b128 v[162:165], v241 offset:35840
	ds_read_b128 v[166:169], v241 offset:49152
	ds_read_b128 v[170:173], v241 offset:50176
	ds_read_b128 v[174:177], v241 offset:51200
	ds_read_b128 v[178:181], v241 offset:52224
	s_mov_b32 m0, s73
	ds_read_b128 v[182:185], v148 offset:32768
	ds_read_b128 v[202:205], v148 offset:33792
	ds_read_b128 v[206:209], v148 offset:34816
	ds_read_b128 v[214:217], v148 offset:35840
	ds_read_b128 v[218:221], v148 offset:36864
	ds_read_b128 v[222:225], v148 offset:37888
	ds_read_b128 v[226:229], v148 offset:38912
	ds_read_b128 v[230:233], v148 offset:39936
	global_load_lds_dwordx4 v142, s[16:17]
	s_mov_b32 m0, s90
	s_nop 0
	global_load_lds_dwordx4 v140, s[16:17]
	s_waitcnt vmcnt(8)
	s_waitcnt lgkmcnt(0)
	s_barrier
; #define PG8_STAGE(bufoff, gbase, voff) do { _Pragma("unroll") for (int _i = 0; _i < 2; ++_i) \
;         __builtin_amdgcn_global_load_lds((const unsigned*)((const char*)(gbase) + (voff)[_i]), (LAS unsigned*)(lds + (bufoff) + ldsw + _i * 8192), 16, 0, 0); } while (0)
; #define PG8_LDA(dst, b, h) do { _Pragma("unroll") for (int m = 0; m < 4; ++m) _Pragma("unroll") for (int k = 0; k < 2; ++k) dst[m][k] = *(const LAS bf16x8*)(lds + PG8_SA(b, h) + aoff + m * 2048 + k * 1024); } while (0)
; #define PG8_MMA(ai, bj, At, Bt) do { __builtin_amdgcn_s_setprio(1); _Pragma("unroll") for (int m = 0; m < 4; ++m) _Pragma("unroll") for (int n = 0; n < 2; ++n) _Pragma("unroll") for (int k = 0; k < 2; ++k) \
;         acc[ai][bj][m][n] = __builtin_amdgcn_mfma_f32_16x16x32_bf16(Bt[n][k], At[m][k], acc[ai][bj][m][n], 0, 0, 0); __builtin_amdgcn_s_setprio(0); } while (0)
; #define PG8_WAIT_V(n) asm volatile("s_waitcnt vmcnt(" #n ")" ::: "memory")
; #define PG8_WAIT_L(n) asm volatile("s_waitcnt lgkmcnt(" #n ")" ::: "memory")
; #define PG8_BAR __builtin_amdgcn_s_barrier()
; #define PG8_SCHED __builtin_amdgcn_sched_barrier(0)
; template <class Epi, class Sched>
; __device__ __forceinline__ void gemm_phase(LAS unsigned char* lds, const int tid, const char* Abase, const int K, const Sched& S, const Epi& E) {
;     ...
;             PG8_WAIT_V(8); PG8_WAIT_L(0); PG8_BAR; PG8_MMA(0, 0, At, B0); PG8_MMA(0, 1, At, B1); PG8_BAR; PG8_SCHED;
;             PG8_LDA(At, 1, 1); PG8_STAGE(PG8_SB(1, 0), b3, voffB); PG8_STAGE(PG8_SB(1, 1), b3 + hstep, voffB); PG8_STAGE(PG8_SA(1, 0), a3, w2[0]);
;             PG8_WAIT_V(8); PG8_WAIT_L(0); PG8_BAR; PG8_MMA(1, 0, At, B0); PG8_MMA(1, 1, At, B1); PG8_BAR; PG8_SCHED;
	s_setprio 1
	s_waitcnt lgkmcnt(0)
	v_mfma_f32_16x16x32_bf16 v[130:133], v[150:153], v[182:185], v[130:133]
	v_mfma_f32_16x16x32_bf16 v[126:129], v[158:161], v[182:185], v[126:129]
	v_mfma_f32_16x16x32_bf16 v[110:113], v[150:153], v[206:209], v[110:113]
	v_mfma_f32_16x16x32_bf16 v[106:109], v[158:161], v[206:209], v[106:109]
	v_mfma_f32_16x16x32_bf16 v[94:97], v[150:153], v[218:221], v[94:97]
	v_mfma_f32_16x16x32_bf16 v[90:93], v[158:161], v[218:221], v[90:93]
	v_mfma_f32_16x16x32_bf16 v[78:81], v[150:153], v[226:229], v[78:81]
	v_mfma_f32_16x16x32_bf16 v[74:77], v[158:161], v[226:229], v[74:77]
	v_mfma_f32_16x16x32_bf16 v[130:133], v[154:157], v[202:205], v[130:133]
	v_mfma_f32_16x16x32_bf16 v[126:129], v[162:165], v[202:205], v[126:129]
	v_mfma_f32_16x16x32_bf16 v[110:113], v[154:157], v[214:217], v[110:113]
	v_mfma_f32_16x16x32_bf16 v[106:109], v[162:165], v[214:217], v[106:109]
	v_mfma_f32_16x16x32_bf16 v[94:97], v[154:157], v[222:225], v[94:97]
	v_mfma_f32_16x16x32_bf16 v[90:93], v[162:165], v[222:225], v[90:93]
	v_mfma_f32_16x16x32_bf16 v[78:81], v[154:157], v[230:233], v[78:81]
	v_mfma_f32_16x16x32_bf16 v[74:77], v[162:165], v[230:233], v[74:77]
	s_setprio 0
	s_setprio 1
	v_mfma_f32_16x16x32_bf16 v[122:125], v[166:169], v[182:185], v[122:125]
	v_mfma_f32_16x16x32_bf16 v[118:121], v[174:177], v[182:185], v[118:121]
	v_mfma_f32_16x16x32_bf16 v[102:105], v[166:169], v[206:209], v[102:105]
	v_mfma_f32_16x16x32_bf16 v[98:101], v[174:177], v[206:209], v[98:101]
	v_mfma_f32_16x16x32_bf16 v[86:89], v[166:169], v[218:221], v[86:89]
	v_mfma_f32_16x16x32_bf16 v[82:85], v[174:177], v[218:221], v[82:85]
	v_mfma_f32_16x16x32_bf16 v[70:73], v[166:169], v[226:229], v[70:73]
	v_mfma_f32_16x16x32_bf16 v[66:69], v[174:177], v[226:229], v[66:69]
	v_mfma_f32_16x16x32_bf16 v[122:125], v[170:173], v[202:205], v[122:125]
	v_mfma_f32_16x16x32_bf16 v[118:121], v[178:181], v[202:205], v[118:121]
	v_mfma_f32_16x16x32_bf16 v[102:105], v[170:173], v[214:217], v[102:105]
	v_mfma_f32_16x16x32_bf16 v[98:101], v[178:181], v[214:217], v[98:101]
	v_mfma_f32_16x16x32_bf16 v[86:89], v[170:173], v[222:225], v[86:89]
	v_mfma_f32_16x16x32_bf16 v[82:85], v[178:181], v[222:225], v[82:85]
	v_mfma_f32_16x16x32_bf16 v[70:73], v[170:173], v[230:233], v[70:73]
	v_mfma_f32_16x16x32_bf16 v[66:69], v[178:181], v[230:233], v[66:69]
	s_setprio 0
	s_barrier
	s_add_u32 s100, s16, s24
	s_addc_u32 s101, s17, s25
	s_add_u32 s14, s14, s24
	s_addc_u32 s15, s15, s25
	s_add_i32 s16, s20, s70
	s_mov_b32 m0, s16
	ds_read_b128 v[140:143], v148 offset:49152
	ds_read_b128 v[182:185], v148 offset:50176
	ds_read_b128 v[202:205], v148 offset:51200
	ds_read_b128 v[206:209], v148 offset:52224
	ds_read_b128 v[214:217], v148 offset:53248
	ds_read_b128 v[218:221], v148 offset:54272
	ds_read_b128 v[222:225], v148 offset:55296
	ds_read_b128 v[226:229], v148 offset:56320
	global_load_lds_dwordx4 v134, s[14:15]
	s_add_i32 m0, s16, 0x2000
	s_nop 0
	global_load_lds_dwordx4 v136, s[14:15]
	s_add_u32 s14, s14, 0x40000
	s_addc_u32 s15, s15, 0
	s_add_i32 s16, s21, s70
	s_mov_b32 m0, s16
	s_nop 0
	global_load_lds_dwordx4 v134, s[14:15]
	s_add_i32 m0, s16, 0x2000
	s_nop 0
	global_load_lds_dwordx4 v136, s[14:15]
	s_mov_b32 m0, s2
	s_nop 0
	global_load_lds_dwordx4 v0, s[100:101]
	s_mov_b32 m0, s33
	s_nop 0
	global_load_lds_dwordx4 v144, s[100:101]
	s_waitcnt vmcnt(8)
	s_waitcnt lgkmcnt(0)
	s_barrier
	s_setprio 1
	s_waitcnt lgkmcnt(0)
	v_mfma_f32_16x16x32_bf16 v[62:65], v[150:153], v[140:143], v[62:65]
	v_mfma_f32_16x16x32_bf16 v[58:61], v[158:161], v[140:143], v[58:61]
	v_mfma_f32_16x16x32_bf16 v[46:49], v[150:153], v[202:205], v[46:49]
	v_mfma_f32_16x16x32_bf16 v[42:45], v[158:161], v[202:205], v[42:45]
	v_mfma_f32_16x16x32_bf16 v[30:33], v[150:153], v[214:217], v[30:33]
	v_mfma_f32_16x16x32_bf16 v[26:29], v[158:161], v[214:217], v[26:29]
	v_mfma_f32_16x16x32_bf16 v[14:17], v[150:153], v[222:225], v[14:17]
	v_mfma_f32_16x16x32_bf16 v[10:13], v[158:161], v[222:225], v[10:13]
	v_mfma_f32_16x16x32_bf16 v[62:65], v[154:157], v[182:185], v[62:65]
	v_mfma_f32_16x16x32_bf16 v[58:61], v[162:165], v[182:185], v[58:61]
	v_mfma_f32_16x16x32_bf16 v[46:49], v[154:157], v[206:209], v[46:49]
	v_mfma_f32_16x16x32_bf16 v[42:45], v[162:165], v[206:209], v[42:45]
	v_mfma_f32_16x16x32_bf16 v[30:33], v[154:157], v[218:221], v[30:33]
	v_mfma_f32_16x16x32_bf16 v[26:29], v[162:165], v[218:221], v[26:29]
	v_mfma_f32_16x16x32_bf16 v[14:17], v[154:157], v[226:229], v[14:17]
	v_mfma_f32_16x16x32_bf16 v[10:13], v[162:165], v[226:229], v[10:13]
	s_setprio 0
	s_setprio 1
	v_mfma_f32_16x16x32_bf16 v[54:57], v[166:169], v[140:143], v[54:57]
	v_mfma_f32_16x16x32_bf16 v[50:53], v[174:177], v[140:143], v[50:53]
	v_mfma_f32_16x16x32_bf16 v[38:41], v[166:169], v[202:205], v[38:41]
	v_mfma_f32_16x16x32_bf16 v[34:37], v[174:177], v[202:205], v[34:37]
	v_mfma_f32_16x16x32_bf16 v[22:25], v[166:169], v[214:217], v[22:25]
	v_mfma_f32_16x16x32_bf16 v[18:21], v[174:177], v[214:217], v[18:21]
	v_mfma_f32_16x16x32_bf16 v[6:9], v[166:169], v[222:225], v[6:9]
	v_mfma_f32_16x16x32_bf16 v[2:5], v[174:177], v[222:225], v[2:5]
	v_mfma_f32_16x16x32_bf16 v[54:57], v[170:173], v[182:185], v[54:57]
	v_mfma_f32_16x16x32_bf16 v[50:53], v[178:181], v[182:185], v[50:53]
	v_mfma_f32_16x16x32_bf16 v[38:41], v[170:173], v[206:209], v[38:41]
	v_mfma_f32_16x16x32_bf16 v[34:37], v[178:181], v[206:209], v[34:37]
	v_mfma_f32_16x16x32_bf16 v[22:25], v[170:173], v[218:221], v[22:25]
	v_mfma_f32_16x16x32_bf16 v[18:21], v[178:181], v[218:221], v[18:21]
	v_mfma_f32_16x16x32_bf16 v[6:9], v[170:173], v[226:229], v[6:9]
	v_mfma_f32_16x16x32_bf16 v[2:5], v[178:181], v[226:229], v[2:5]
	s_setprio 0
	s_barrier
	s_add_i32 s19, s19, 2
	s_add_u32 s7, s7, 0x100
	s_addc_u32 s18, s18, 0
	s_add_u32 s12, s12, 0x100
	s_addc_u32 s13, s13, 0
	s_cmp_gt_u32 s19, 13
	s_cbranch_scc1 .LBB0_350
